# speedup vs baseline: 1.0175x; 1.0108x over previous
_Z11prep_kernel7CvtArgsPKiPj6LnArgs:
	s_load_dwordx8 s[20:27], s[0:1], 0x88
	s_load_dwordx4 s[28:31], s[0:1], 0xa8
	s_cmpk_lt_u32 s2, 0x700
	s_mov_b64 s[4:5], -1
	v_and_b32_e32 v82, 0x3ff, v0
	s_cbranch_scc0 .LBB0_105
	s_load_dwordx4 s[8:11], s[0:1], 0x48
	s_load_dwordx2 s[18:19], s[0:1], 0x28
	s_load_dwordx4 s[4:7], s[0:1], 0x0
	s_load_dwordx4 s[12:15], s[0:1], 0x18
	s_load_dwordx2 s[48:49], s[0:1], 0x80
	s_waitcnt lgkmcnt(0)
	v_lshlrev_b32_e32 v112, 4, v82
	v_lshl_add_u32 v112, s2, 12, v112
	s_add_u32 s50, s48, 0x700000
	s_addc_u32 s51, s49, 0
	s_add_u32 s52, s48, 0xe00000
	s_addc_u32 s53, s49, 0
	global_load_dwordx4 v[100:103], v112, s[48:49] sc0 sc1 nt
	global_load_dwordx4 v[104:107], v112, s[50:51] sc0 sc1 nt
	s_cmpk_lt_u32 s2, 0x200
	s_cbranch_scc0 .Lprep_m3_skip
	global_load_dwordx4 v[108:111], v112, s[52:53] sc0 sc1 nt
.Lprep_m3_skip:
	s_cmp_lg_u32 s2, 0
	s_cbranch_scc1 .Lprep_noslot
	s_add_u32 s54, s14, 0xe3a0100
	s_addc_u32 s55, s15, 0
	v_mov_b32_e32 v114, s6
	v_mov_b32_e32 v115, s7
	v_mov_b32_e32 v116, s12
	v_mov_b32_e32 v117, s13
	v_mov_b32_e32 v118, 0
	global_store_dwordx4 v118, v[114:117], s[54:55]
.Lprep_noslot:
	s_sub_u32 s3, s2, 0x180
	s_cmpk_lt_u32 s3, 0x280
	s_cbranch_scc0 .Lprep_docvt
	v_mbcnt_lo_u32_b32 v70, -1, 0
	v_mbcnt_hi_u32_b32 v70, -1, v70
	s_waitcnt vmcnt(0)
	s_branch .Lprep_maskchk

.LBB0_9:
	s_and_b64 s[8:9], s[38:39], exec
	s_waitcnt lgkmcnt(0)
	s_cselect_b32 s3, s6, s12
	s_cselect_b32 s8, s7, s13
	s_and_b64 s[6:7], s[36:37], exec
	s_cselect_b32 s6, s5, s8
	s_cselect_b32 s3, s4, s3
	s_ashr_i32 s43, s42, 31
	s_lshl_b64 s[4:5], s[42:43], 16
	s_add_u32 s4, s3, s4
	s_addc_u32 s5, s6, s5
	v_mov_b32_e32 v75, 0
	v_lshlrev_b32_e32 v74, 4, v82
	v_lshl_add_u64 v[6:7], s[4:5], 0, v[74:75]
	s_movk_i32 s3, 0x2000
	v_add_co_u32_e32 v2, vcc, s3, v6
	s_movk_i32 s3, 0x4000
	s_nop 0
	v_addc_co_u32_e32 v3, vcc, 0, v7, vcc
	global_load_dwordx4 v[58:61], v[2:3], off offset:-4096 sc0 sc1 nt
	global_load_dwordx4 v[54:57], v[2:3], off sc0 sc1 nt
	v_add_co_u32_e32 v2, vcc, s3, v6
	s_movk_i32 s3, 0x6000
	s_nop 0
	v_addc_co_u32_e32 v3, vcc, 0, v7, vcc
	global_load_dwordx4 v[50:53], v[2:3], off offset:-4096 sc0 sc1 nt
	global_load_dwordx4 v[46:49], v[2:3], off sc0 sc1 nt
	v_add_co_u32_e32 v2, vcc, s3, v6
	s_mov_b32 s3, 0x8000
	s_nop 0
	v_addc_co_u32_e32 v3, vcc, 0, v7, vcc
	global_load_dwordx4 v[42:45], v[2:3], off offset:-4096 sc0 sc1 nt
	global_load_dwordx4 v[38:41], v[2:3], off sc0 sc1 nt
	v_add_co_u32_e32 v2, vcc, s3, v6
	s_mov_b32 s3, 0xa000
	s_nop 0
	v_addc_co_u32_e32 v3, vcc, 0, v7, vcc
	global_load_dwordx4 v[34:37], v[2:3], off offset:-4096 sc0 sc1 nt
	global_load_dwordx4 v[30:33], v[2:3], off sc0 sc1 nt
	v_add_co_u32_e32 v2, vcc, s3, v6
	s_mov_b32 s3, 0xc000
	s_nop 0
	v_addc_co_u32_e32 v3, vcc, 0, v7, vcc
	global_load_dwordx4 v[26:29], v[2:3], off offset:-4096 sc0 sc1 nt
	global_load_dwordx4 v[22:25], v[2:3], off sc0 sc1 nt
	v_add_co_u32_e32 v2, vcc, s3, v6
	s_mov_b32 s3, 0xd000
	s_nop 0
	v_addc_co_u32_e32 v3, vcc, 0, v7, vcc
	v_add_co_u32_e32 v8, vcc, s3, v6
	global_load_dwordx4 v[18:21], v[2:3], off offset:-4096 sc0 sc1 nt
	global_load_dwordx4 v[10:13], v[2:3], off sc0 sc1 nt
	v_addc_co_u32_e32 v9, vcc, 0, v7, vcc
	v_add_co_u32_e32 v62, vcc, 0xe000, v6
	v_lshlrev_b32_e32 v1, 2, v82
	s_nop 0
	v_addc_co_u32_e32 v63, vcc, 0, v7, vcc
	v_add_co_u32_e32 v66, vcc, 0xf000, v6
	global_load_dwordx4 v[14:17], v[8:9], off sc0 sc1 nt
	global_load_dwordx4 v[2:5], v[62:63], off sc0 sc1 nt
	v_addc_co_u32_e32 v67, vcc, 0, v7, vcc
	global_load_dwordx4 v[62:65], v74, s[4:5] sc0 sc1 nt
	global_load_dwordx4 v[6:9], v[66:67], off sc0 sc1 nt
	s_andn2_b64 vcc, exec, s[10:11]
	s_cbranch_vccnz .LBB0_29
	s_load_dwordx8 s[4:11], s[0:1], 0x60
	v_lshlrev_b32_e32 v74, 2, v1
	v_mbcnt_lo_u32_b32 v83, -1, 0
	v_mbcnt_hi_u32_b32 v94, -1, v83
	v_and_b32_e32 v83, 64, v94
	s_waitcnt lgkmcnt(0)
	v_lshl_add_u64 v[76:77], s[4:5], 0, v[74:75]
	global_load_dwordx4 v[70:73], v74, s[6:7]
	global_load_dwordx4 v[66:69], v74, s[4:5]
	v_lshl_add_u64 v[74:75], s[6:7], 0, v[74:75]
	v_add_co_u32_e32 v76, vcc, 0x1000, v76
	s_mov_b64 s[4:5], vcc
	v_add_co_u32_e32 v74, vcc, 0x1000, v74
	v_xor_b32_e32 v84, 32, v94
	s_nop 0
	v_addc_co_u32_e32 v75, vcc, 0, v75, vcc
	v_addc_co_u32_e64 v77, vcc, 0, v77, s[4:5]
	global_load_dwordx4 v[78:81], v[74:75], off
	v_add_u32_e32 v95, 64, v83
	global_load_dwordx4 v[74:77], v[76:77], off
	v_cmp_lt_i32_e32 vcc, v84, v95
	s_waitcnt vmcnt(3)
	v_pk_mul_f32 v[86:87], v[70:71], v[62:63]
	v_cndmask_b32_e32 v83, v94, v84, vcc
	v_pk_mul_f32 v[84:85], v[72:73], v[64:65]
	s_waitcnt vmcnt(2)
	v_pk_mul_f32 v[64:65], v[68:69], v[64:65]
	v_pk_mul_f32 v[62:63], v[66:67], v[62:63]
	v_mov_b32_e32 v89, v86
	v_mov_b32_e32 v88, v62
	v_mov_b32_e32 v86, v63
	v_mov_b32_e32 v90, v64
	v_mov_b32_e32 v91, v84
	v_mov_b32_e32 v84, v65
	v_pk_add_f32 v[86:87], v[88:89], v[86:87]
	v_pk_add_f32 v[84:85], v[90:91], v[84:85]
	s_waitcnt vmcnt(1)
	v_pk_mul_f32 v[88:89], v[78:79], v[58:59]
	v_pk_add_f32 v[84:85], v[86:87], v[84:85]
	v_pk_mul_f32 v[86:87], v[80:81], v[60:61]
	s_waitcnt vmcnt(0)
	v_pk_mul_f32 v[60:61], v[76:77], v[60:61]
	v_pk_mul_f32 v[58:59], v[74:75], v[58:59]
	v_mov_b32_e32 v91, v88
	v_mov_b32_e32 v90, v58
	v_mov_b32_e32 v88, v59
	v_mov_b32_e32 v92, v60
	v_mov_b32_e32 v93, v86
	v_mov_b32_e32 v86, v61
	v_pk_add_f32 v[88:89], v[90:91], v[88:89]
	v_pk_add_f32 v[86:87], v[92:93], v[86:87]
	v_lshlrev_b32_e32 v83, 2, v83
	v_pk_add_f32 v[86:87], v[88:89], v[86:87]
	v_xor_b32_e32 v88, 16, v94
	v_pk_add_f32 v[84:85], v[84:85], v[86:87]
	ds_bpermute_b32 v86, v83, v84
	ds_bpermute_b32 v87, v83, v85
	v_cmp_lt_i32_e32 vcc, v88, v95
	v_xor_b32_e32 v89, 8, v94
	v_xor_b32_e32 v90, 4, v94
	v_cndmask_b32_e32 v88, v94, v88, vcc
	v_lshlrev_b32_e32 v88, 2, v88
	s_waitcnt lgkmcnt(0)
	v_pk_add_f32 v[84:85], v[84:85], v[86:87]
	ds_bpermute_b32 v86, v88, v84
	ds_bpermute_b32 v87, v88, v85
	v_cmp_lt_i32_e32 vcc, v89, v95
	v_xor_b32_e32 v91, 2, v94
	v_xor_b32_e32 v92, 1, v94
	v_cndmask_b32_e32 v89, v94, v89, vcc
	v_lshlrev_b32_e32 v89, 2, v89
	s_waitcnt lgkmcnt(0)
	v_pk_add_f32 v[84:85], v[84:85], v[86:87]
	ds_bpermute_b32 v86, v89, v84
	ds_bpermute_b32 v87, v89, v85
	v_cmp_lt_i32_e32 vcc, v90, v95
	s_waitcnt lgkmcnt(0)
	v_pk_add_f32 v[84:85], v[84:85], v[86:87]
	v_cndmask_b32_e32 v90, v94, v90, vcc
	v_lshlrev_b32_e32 v90, 2, v90
	ds_bpermute_b32 v86, v90, v84
	ds_bpermute_b32 v87, v90, v85
	v_cmp_lt_i32_e32 vcc, v91, v95
	s_waitcnt lgkmcnt(0)
	v_pk_add_f32 v[84:85], v[84:85], v[86:87]
	v_cndmask_b32_e32 v91, v94, v91, vcc
	v_lshlrev_b32_e32 v91, 2, v91
	ds_bpermute_b32 v86, v91, v84
	ds_bpermute_b32 v87, v91, v85
	v_cmp_lt_i32_e32 vcc, v92, v95
	s_waitcnt lgkmcnt(0)
	v_pk_add_f32 v[84:85], v[84:85], v[86:87]
	v_cndmask_b32_e32 v92, v94, v92, vcc
	v_lshlrev_b32_e32 v93, 2, v92
	ds_bpermute_b32 v86, v93, v84
	ds_bpermute_b32 v87, v93, v85
	v_and_b32_e32 v92, 63, v82
	v_cmp_eq_u32_e32 vcc, 0, v92
	v_lshrrev_b32_e32 v92, 3, v82
	s_and_saveexec_b64 s[4:5], vcc
	s_cbranch_execz .LBB0_12
	s_waitcnt lgkmcnt(0)
	v_pk_add_f32 v[84:85], v[84:85], v[86:87]
	ds_write_b64 v92, v[84:85] offset:16384

.Lprep_maskchk:
	s_mov_b32 s3, 0
	v_mov_b32_e32 v83, 0
	v_lshl_add_u32 v2, s2, 8, v82
	v_lshrrev_b32_e32 v8, 9, v2
	v_and_b32_e32 v2, 0x1ff, v2
	v_lshlrev_b32_e32 v2, 2, v2
	v_or_b32_e32 v9, 2, v2
	v_or_b32_e32 v5, 3, v2
	v_cmp_gt_u32_e32 vcc, v2, v8
	v_cmp_ge_u32_e64 s[4:5], v2, v8
	v_cmp_gt_u32_e64 s[8:9], v9, v8
	v_cmp_gt_u32_e64 s[10:11], v5, v8
	v_cmp_ne_u32_e64 s[12:13], 0, v100
	v_cmp_ne_u32_e64 s[14:15], 0, v101
	v_cmp_ne_u32_e64 s[16:17], 0, v102
	v_cmp_ne_u32_e64 s[18:19], 0, v103
	s_nop 1
	s_xor_b64 s[12:13], s[12:13], vcc
	s_xor_b64 s[4:5], s[14:15], s[4:5]
	s_xor_b64 s[8:9], s[16:17], s[8:9]
	s_xor_b64 s[10:11], s[18:19], s[10:11]
	s_or_b64 s[12:13], s[12:13], s[4:5]
	s_or_b64 s[8:9], s[8:9], s[10:11]
	s_or_b64 s[38:39], s[12:13], s[8:9]
	v_add_u32_e32 v8, 0x380, v8
	v_cmp_gt_u32_e32 vcc, v2, v8
	v_cmp_ge_u32_e64 s[4:5], v2, v8
	v_cmp_gt_u32_e64 s[8:9], v9, v8
	v_cmp_gt_u32_e64 s[10:11], v5, v8
	v_cmp_ne_u32_e64 s[12:13], 0, v104
	v_cmp_ne_u32_e64 s[14:15], 0, v105
	v_cmp_ne_u32_e64 s[16:17], 0, v106
	v_cmp_ne_u32_e64 s[18:19], 0, v107
	s_nop 1
	s_xor_b64 s[12:13], s[12:13], vcc
	s_xor_b64 s[4:5], s[14:15], s[4:5]
	s_xor_b64 s[8:9], s[16:17], s[8:9]
	s_xor_b64 s[10:11], s[18:19], s[10:11]
	s_or_b64 s[12:13], s[12:13], s[4:5]
	s_or_b64 s[8:9], s[8:9], s[10:11]
	s_or_b64 s[12:13], s[12:13], s[8:9]
	s_or_b64 s[38:39], s[38:39], s[12:13]
	s_cmpk_lt_u32 s2, 0x200
	s_cbranch_scc0 .Lprep_chk_done
	v_add_u32_e32 v8, 0x380, v8
	v_cmp_gt_u32_e32 vcc, v2, v8
	v_cmp_ge_u32_e64 s[4:5], v2, v8
	v_cmp_gt_u32_e64 s[8:9], v9, v8
	v_cmp_gt_u32_e64 s[10:11], v5, v8
	v_cmp_ne_u32_e64 s[12:13], 0, v108
	v_cmp_ne_u32_e64 s[14:15], 0, v109
	v_cmp_ne_u32_e64 s[16:17], 0, v110
	v_cmp_ne_u32_e64 s[18:19], 0, v111
	s_nop 1
	s_xor_b64 s[12:13], s[12:13], vcc
	s_xor_b64 s[4:5], s[14:15], s[4:5]
	s_xor_b64 s[8:9], s[16:17], s[8:9]
	s_xor_b64 s[10:11], s[18:19], s[10:11]
	s_or_b64 s[12:13], s[12:13], s[4:5]
	s_or_b64 s[8:9], s[8:9], s[10:11]
	s_or_b64 s[12:13], s[12:13], s[8:9]
	s_or_b64 s[38:39], s[38:39], s[12:13]

.LBB0_108:
	s_or_b64 exec, exec, s[2:3]
	v_lshlrev_b32_e32 v32, 4, v82
	v_mov_b32_e32 v33, 0
	v_lshl_add_u64 v[0:1], s[24:25], 0, v[32:33]
	s_movk_i32 s0, 0x1000
	v_add_co_u32_e32 v0, vcc, s0, v0
	v_lshl_add_u64 v[12:13], s[26:27], 0, v[32:33]
	s_nop 0
	v_addc_co_u32_e32 v1, vcc, 0, v1, vcc
	global_load_dwordx4 v[100:103], v[0:1], off
	s_nop 0
	global_load_dwordx4 v[104:107], v32, s[24:25]
	global_load_dwordx4 v[108:111], v32, s[26:27]
	v_add_co_u32_e32 v12, vcc, s0, v12
	v_lshrrev_b32_e32 v16, 6, v82
	s_nop 0
	v_addc_co_u32_e32 v13, vcc, 0, v13, vcc
	global_load_dwordx4 v[112:115], v[12:13], off
	v_lshl_add_u32 v34, s4, 2, v16
	v_ashrrev_i32_e32 v35, 31, v34
	v_lshlrev_b64 v[16:17], 13, v[34:35]
	v_lshl_add_u64 v[16:17], s[22:23], 0, v[16:17]
	v_mbcnt_lo_u32_b32 v35, -1, 0
	v_mbcnt_hi_u32_b32 v35, -1, v35
	v_xor_b32_e32 v56, 16, v35
	v_xor_b32_e32 v57, 8, v35
	v_xor_b32_e32 v58, 4, v35
	s_mov_b32 s2, 0x800000
	s_movk_i32 s3, 0x1080
	v_mov_b32_e32 v116, v32
	v_and_b32_e32 v32, 0x3f0, v32
	v_lshl_add_u64 v[0:1], v[16:17], 0, v[32:33]
	global_load_dwordx4 v[28:31], v[0:1], off sc0 sc1 nt
	global_load_dwordx4 v[24:27], v[0:1], off offset:1024 sc0 sc1 nt
	global_load_dwordx4 v[20:23], v[0:1], off offset:2048 sc0 sc1 nt
	global_load_dwordx4 v[16:19], v[0:1], off offset:3072 sc0 sc1 nt
	v_add_co_u32_e32 v36, vcc, s0, v0
	s_nop 1
	v_addc_co_u32_e32 v37, vcc, 0, v1, vcc
	global_load_dwordx4 v[12:15], v[36:37], off sc0 sc1 nt
	global_load_dwordx4 v[8:11], v[36:37], off offset:1024 sc0 sc1 nt
	global_load_dwordx4 v[4:7], v[36:37], off offset:2048 sc0 sc1 nt
	global_load_dwordx4 v[0:3], v[36:37], off offset:3072 sc0 sc1 nt
	s_waitcnt vmcnt(8)
	ds_write_b128 v116, v[104:107]
	ds_write_b128 v116, v[108:111] offset:8192
	ds_write_b128 v116, v[100:103] offset:4096
	ds_write_b128 v116, v[112:115] offset:12288
	s_waitcnt vmcnt(7)
	v_mov_b32_e32 v38, v29
	v_and_b32_e32 v36, 64, v35
	v_xor_b32_e32 v37, 32, v35
	v_add_u32_e32 v59, 64, v36
	v_cmp_lt_i32_e32 vcc, v37, v59
	s_waitcnt vmcnt(6)
	v_mov_b32_e32 v39, v25
	v_mov_b32_e32 v40, v30
	v_cndmask_b32_e32 v36, v35, v37, vcc
	v_lshlrev_b32_e32 v83, 2, v36
	v_mov_b32_e32 v36, v28
	v_mov_b32_e32 v37, v24
	v_mov_b32_e32 v41, v26
	v_mov_b32_e32 v42, v31
	v_mov_b32_e32 v43, v27
	s_waitcnt vmcnt(5)
	v_mov_b32_e32 v44, v21
	v_mov_b32_e32 v45, v22
	v_mov_b32_e32 v46, v20
	v_mov_b32_e32 v47, v23
	v_pk_add_f32 v[36:37], v[36:37], v[38:39]
	v_pk_add_f32 v[38:39], v[40:41], v[42:43]
	v_pk_add_f32 v[40:41], v[44:45], v[46:47]
	v_pk_add_f32 v[36:37], v[36:37], v[38:39]
	v_pk_add_f32 v[38:39], v[40:41], v[40:41] op_sel:[0,1] op_sel_hi:[1,0]
	v_add_f32_e32 v36, 0, v36
	s_waitcnt vmcnt(4)
	v_add_f32_e32 v48, v16, v17
	v_add_f32_e32 v50, v18, v19
	v_add_f32_e32 v42, v36, v37
	v_cmp_lt_i32_e32 vcc, v56, v59
	s_waitcnt lgkmcnt(0)
	s_barrier
	s_waitcnt vmcnt(3)
	v_mov_b32_e32 v43, v12
	v_mov_b32_e32 v49, v14
	v_mov_b32_e32 v51, v15
	v_mov_b32_e32 v39, v13
	s_waitcnt vmcnt(2)
	v_mov_b32_e32 v44, v9
	v_mov_b32_e32 v45, v10
	v_mov_b32_e32 v46, v8
	v_mov_b32_e32 v47, v11
	v_pk_add_f32 v[40:41], v[48:49], v[50:51]
	v_pk_add_f32 v[36:37], v[42:43], v[38:39]
	v_pk_add_f32 v[44:45], v[44:45], v[46:47]
	v_pk_add_f32 v[36:37], v[36:37], v[40:41]
	v_pk_add_f32 v[44:45], v[44:45], v[44:45] op_sel:[0,1] op_sel_hi:[1,0]
	v_pk_add_f32 v[36:37], v[36:37], v[36:37] op_sel:[0,1] op_sel_hi:[1,0]
	s_waitcnt vmcnt(1)
	v_add_f32_e32 v52, v4, v5
	v_add_f32_e32 v54, v6, v7
	s_waitcnt vmcnt(0)
	v_mov_b32_e32 v53, v2
	v_mov_b32_e32 v55, v3
	v_mov_b32_e32 v45, v1
	v_mov_b32_e32 v37, v0
	v_pk_add_f32 v[46:47], v[52:53], v[54:55]
	v_pk_add_f32 v[36:37], v[36:37], v[44:45]
	v_cndmask_b32_e32 v39, v35, v56, vcc
	v_pk_add_f32 v[36:37], v[36:37], v[46:47]
	v_lshlrev_b32_e32 v93, 2, v39
	v_add_f32_e32 v36, v36, v37
	ds_bpermute_b32 v37, v83, v36
	v_cmp_lt_i32_e32 vcc, v57, v59
	v_xor_b32_e32 v38, 2, v35
	v_xor_b32_e32 v39, 1, v35
	v_cndmask_b32_e32 v40, v35, v57, vcc
	s_waitcnt lgkmcnt(0)
	v_add_f32_e32 v36, v36, v37
	ds_bpermute_b32 v37, v93, v36
	v_lshlrev_b32_e32 v96, 2, v40
	v_cmp_lt_i32_e32 vcc, v58, v59
	v_mov_b32_e32 v46, v22
	v_mov_b32_e32 v56, v28
	s_waitcnt lgkmcnt(0)
	v_add_f32_e32 v36, v36, v37
	ds_bpermute_b32 v37, v96, v36
	v_cndmask_b32_e32 v40, v35, v58, vcc
	v_lshlrev_b32_e32 v97, 2, v40
	v_cmp_lt_i32_e32 vcc, v38, v59
	v_mov_b32_e32 v40, v10
	s_waitcnt lgkmcnt(0)
	v_add_f32_e32 v36, v36, v37
	ds_bpermute_b32 v37, v97, v36
	v_cndmask_b32_e32 v38, v35, v38, vcc
	v_lshlrev_b32_e32 v98, 2, v38
	v_cmp_lt_i32_e32 vcc, v39, v59
	v_mov_b32_e32 v58, v24
	s_waitcnt lgkmcnt(0)
	v_add_f32_e32 v36, v36, v37
	ds_bpermute_b32 v37, v98, v36
	v_cndmask_b32_e32 v35, v35, v39, vcc
	v_lshlrev_b32_e32 v35, 2, v35
	v_mov_b32_e32 v52, v18
	v_mov_b32_e32 v48, v12
	s_waitcnt lgkmcnt(0)
	v_add_f32_e32 v37, v36, v37
	ds_bpermute_b32 v39, v35, v37
	v_mov_b32_e32 v38, v6
	v_mov_b32_e32 v36, v0
	s_waitcnt lgkmcnt(0)
	v_add_f32_e32 v44, v37, v39
	v_fmamk_f32 v63, v44, 0xba000000, v21
	v_fmamk_f32 v62, v44, 0xba000000, v20
	v_fmamk_f32 v47, v44, 0xba000000, v23
	v_fmac_f32_e32 v46, 0xba000000, v44
	v_fmamk_f32 v51, v44, 0xba000000, v9
	v_fmamk_f32 v50, v44, 0xba000000, v8
	v_fmamk_f32 v41, v44, 0xba000000, v11
	v_fmac_f32_e32 v40, 0xba000000, v44
	v_fmamk_f32 v57, v44, 0xba000000, v29
	v_fmamk_f32 v59, v44, 0xba000000, v25
	v_fmamk_f32 v65, v44, 0xba000000, v31
	v_fmamk_f32 v67, v44, 0xba000000, v27
	v_fmac_f32_e32 v56, 0xba000000, v44
	v_fmac_f32_e32 v58, 0xba000000, v44
	v_fmamk_f32 v64, v44, 0xba000000, v30
	v_fmamk_f32 v66, v44, 0xba000000, v26
	v_pk_mul_f32 v[68:69], v[46:47], v[46:47]
	v_pk_mul_f32 v[70:71], v[62:63], v[62:63]
	v_pk_mul_f32 v[72:73], v[40:41], v[40:41]
	v_pk_mul_f32 v[74:75], v[50:51], v[50:51]
	v_mov_b32_e32 v78, v57
	v_mov_b32_e32 v79, v59
	v_mov_b32_e32 v84, v65
	v_mov_b32_e32 v85, v67
	v_mov_b32_e32 v76, v56
	v_mov_b32_e32 v77, v58
	v_mov_b32_e32 v80, v64
	v_mov_b32_e32 v81, v66
	v_pk_mov_b32 v[94:95], v[70:71], v[68:69] op_sel:[1,0]
	v_mov_b32_e32 v71, v69
	v_pk_mov_b32 v[68:69], v[74:75], v[72:73] op_sel:[1,0]
	v_mov_b32_e32 v75, v73
	v_pk_mul_f32 v[72:73], v[78:79], v[78:79]
	v_pk_mul_f32 v[78:79], v[84:85], v[84:85]
	v_fmamk_f32 v60, v44, 0xba000000, v16
	v_fmac_f32_e32 v52, 0xba000000, v44
	v_pk_fma_f32 v[72:73], v[76:77], v[76:77], v[72:73]
	v_pk_fma_f32 v[76:77], v[80:81], v[80:81], v[78:79]
	v_fmamk_f32 v61, v44, 0xba000000, v17
	v_fmamk_f32 v53, v44, 0xba000000, v19
	v_mul_f32_e32 v86, v60, v60
	v_mul_f32_e32 v88, v52, v52
	v_pk_add_f32 v[70:71], v[94:95], v[70:71]
	v_pk_add_f32 v[72:73], v[72:73], v[76:77]
	v_fmamk_f32 v49, v44, 0xba000000, v13
	v_fmac_f32_e32 v48, 0xba000000, v44
	v_fmamk_f32 v55, v44, 0xba000000, v15
	v_fmamk_f32 v54, v44, 0xba000000, v14
	v_pk_fma_f32 v[84:85], v[60:61], v[60:61], v[86:87] op_sel_hi:[1,1,0]
	v_pk_fma_f32 v[86:87], v[52:53], v[52:53], v[88:89] op_sel_hi:[1,1,0]
	v_pk_add_f32 v[70:71], v[70:71], v[70:71] op_sel_hi:[0,1]
	v_pk_add_f32 v[72:73], v[72:73], v[72:73] op_sel_hi:[0,1]
	v_mul_f32_e32 v84, v48, v48
	v_mul_f32_e32 v86, v49, v49
	v_mul_f32_e32 v70, v54, v54
	v_mul_f32_e32 v72, v55, v55
	v_fmamk_f32 v42, v44, 0xba000000, v4
	v_fmac_f32_e32 v38, 0xba000000, v44
	v_pk_add_f32 v[68:69], v[68:69], v[74:75]
	v_pk_add_f32 v[74:75], v[84:85], v[86:87]
	v_pk_add_f32 v[70:71], v[70:71], v[72:73]
	v_fmamk_f32 v43, v44, 0xba000000, v5
	v_fmamk_f32 v39, v44, 0xba000000, v7
	v_mul_f32_e32 v90, v42, v42
	v_mul_f32_e32 v92, v38, v38
	v_pk_add_f32 v[70:71], v[74:75], v[70:71]
	v_fmamk_f32 v37, v44, 0xba000000, v1
	v_fmac_f32_e32 v36, 0xba000000, v44
	v_fmamk_f32 v45, v44, 0xba000000, v3
	v_fmamk_f32 v44, v44, 0xba000000, v2
	v_pk_fma_f32 v[88:89], v[42:43], v[42:43], v[90:91] op_sel_hi:[1,1,0]
	v_pk_fma_f32 v[90:91], v[38:39], v[38:39], v[92:93] op_sel_hi:[1,1,0]
	v_pk_add_f32 v[68:69], v[68:69], v[68:69] op_sel_hi:[0,1]
	v_pk_add_f32 v[70:71], v[70:71], v[70:71] op_sel_hi:[0,1]
	v_mul_f32_e32 v88, v36, v36
	v_mul_f32_e32 v90, v37, v37
	v_mul_f32_e32 v68, v44, v44
	v_mul_f32_e32 v70, v45, v45
	v_pk_add_f32 v[76:77], v[88:89], v[90:91]
	v_pk_add_f32 v[68:69], v[68:69], v[70:71]
	v_mov_b32_e32 v81, v33
	v_pk_add_f32 v[68:69], v[76:77], v[68:69]
	v_mov_b32_e32 v70, 0x3727c5ac
	v_add_f32_e32 v68, v68, v69
	ds_bpermute_b32 v69, v83, v68
	v_lshlrev_b32_e32 v72, 3, v82
	v_and_b32_e32 v79, 1, v82
	v_and_b32_e32 v72, 0x1f0, v72
	v_lshl_or_b32 v80, v79, 9, v72
	s_waitcnt lgkmcnt(0)
	v_add_f32_e32 v68, v68, v69
	ds_bpermute_b32 v69, v93, v68
	v_mov_b32_e32 v78, s28
	s_waitcnt lgkmcnt(0)
	v_add_f32_e32 v69, v68, v69
	ds_bpermute_b32 v71, v96, v69
	v_mov_b32_e32 v68, s30
	s_waitcnt lgkmcnt(0)
	v_add_f32_e32 v71, v69, v71
	ds_bpermute_b32 v73, v97, v71
	v_mov_b32_e32 v69, s31
	v_mad_i64_i32 v[68:69], s[0:1], v34, s3, v[68:69]
	v_lshl_add_u64 v[68:69], v[68:69], 0, v[80:81]
	s_waitcnt lgkmcnt(0)
	v_add_f32_e32 v71, v71, v73
	ds_bpermute_b32 v73, v98, v71
	s_waitcnt lgkmcnt(0)
	v_add_f32_e32 v33, v71, v73
	ds_bpermute_b32 v71, v35, v33
	s_waitcnt lgkmcnt(0)
	v_add_f32_e32 v33, v33, v71
	v_fmac_f32_e32 v70, 0x3a000000, v33
	v_mul_f32_e32 v33, 0x4b800000, v70
	v_cmp_gt_f32_e32 vcc, s2, v70
	s_nop 1
	v_cndmask_b32_e32 v33, v70, v33, vcc
	v_rsq_f32_e32 v33, v33
	ds_read_b128 v[70:73], v32
	ds_read_b128 v[74:77], v32 offset:8192
	v_cvt_pk_f16_f32 v83, v28, v29
	v_cvt_pk_f16_f32 v84, v30, v31
	v_mul_f32_e32 v28, 0x45800000, v33
	v_cndmask_b32_e32 v82, v33, v28, vcc
	v_pk_mul_f32 v[28:29], v[56:57], v[82:83] op_sel_hi:[1,0]
	v_pk_mul_f32 v[30:31], v[64:65], v[82:83] op_sel_hi:[1,0]
	s_waitcnt lgkmcnt(0)
	v_pk_fma_f32 v[28:29], v[70:71], v[28:29], v[74:75]
	v_pk_fma_f32 v[30:31], v[72:73], v[30:31], v[76:77]
	v_pk_mul_f32 v[64:65], v[58:59], v[82:83] op_sel_hi:[1,0]
	v_cvt_pk_bf16_f32 v33, v28, v29
	v_cvt_pk_bf16_f32 v70, v30, v31
	ds_read_b128 v[28:31], v32 offset:1024
	ds_read_b128 v[56:59], v32 offset:9216
	v_pk_mul_f32 v[66:67], v[66:67], v[82:83] op_sel_hi:[1,0]
	v_cmp_eq_u32_e32 vcc, 0, v79
	v_cvt_pk_f16_f32 v71, v24, v25
	v_cvt_pk_f16_f32 v72, v26, v27
	s_waitcnt lgkmcnt(0)
	v_pk_fma_f32 v[24:25], v[30:31], v[66:67], v[58:59]
	v_pk_fma_f32 v[26:27], v[28:29], v[64:65], v[56:57]
	v_cndmask_b32_e32 v59, v83, v71, vcc
	v_cndmask_b32_e32 v64, v84, v72, vcc
	v_cvt_pk_bf16_f32 v56, v26, v27
	v_cvt_pk_bf16_f32 v57, v24, v25
	ds_read_b128 v[24:27], v32 offset:2048
	ds_read_b128 v[28:31], v32 offset:10240
	ds_bpermute_b32 v59, v35, v59
	ds_bpermute_b32 v64, v35, v64
	v_pk_mul_f32 v[62:63], v[62:63], v[82:83] op_sel_hi:[1,0]
	v_pk_mul_f32 v[46:47], v[46:47], v[82:83] op_sel_hi:[1,0]
	v_cndmask_b32_e32 v58, v70, v57, vcc
	v_cndmask_b32_e32 v65, v33, v56, vcc
	s_waitcnt lgkmcnt(2)
	v_pk_fma_f32 v[30:31], v[26:27], v[46:47], v[30:31]
	v_pk_fma_f32 v[28:29], v[24:25], v[62:63], v[28:29]
	s_waitcnt lgkmcnt(1)
	v_cndmask_b32_e32 v26, v71, v59, vcc
	v_cndmask_b32_e32 v24, v59, v83, vcc
	s_waitcnt lgkmcnt(0)
	v_cndmask_b32_e32 v27, v72, v64, vcc
	v_cndmask_b32_e32 v25, v64, v84, vcc
	global_store_dwordx4 v[68:69], v[24:27], off
	ds_bpermute_b32 v24, v35, v65
	ds_bpermute_b32 v25, v35, v58
	v_mov_b32_e32 v79, s29
	v_mad_i64_i32 v[46:47], s[0:1], v34, s3, v[78:79]
	s_waitcnt lgkmcnt(1)
	v_cndmask_b32_e32 v26, v56, v24, vcc
	v_cndmask_b32_e32 v24, v24, v33, vcc
	s_waitcnt lgkmcnt(0)
	v_cndmask_b32_e32 v27, v57, v25, vcc
	v_cndmask_b32_e32 v25, v25, v70, vcc
	v_lshl_add_u64 v[46:47], v[46:47], 0, v[80:81]
	global_store_dwordx4 v[46:47], v[24:27], off
	v_cvt_pk_f16_f32 v33, v20, v21
	v_cvt_pk_f16_f32 v34, v22, v23
	v_cvt_pk_bf16_f32 v56, v28, v29
	v_cvt_pk_bf16_f32 v57, v30, v31
	ds_read_b128 v[20:23], v32 offset:3072
	ds_read_b128 v[24:27], v32 offset:11264
	v_pk_mul_f32 v[28:29], v[60:61], v[82:83] op_sel_hi:[1,0]
	v_pk_mul_f32 v[30:31], v[52:53], v[82:83] op_sel_hi:[1,0]
	s_waitcnt lgkmcnt(0)
	v_pk_fma_f32 v[20:21], v[20:21], v[28:29], v[24:25]
	v_pk_fma_f32 v[22:23], v[22:23], v[30:31], v[26:27]
	v_cvt_pk_f16_f32 v24, v16, v17
	v_cvt_pk_f16_f32 v25, v18, v19
	v_cvt_pk_bf16_f32 v16, v20, v21
	s_nop 0
	v_cvt_pk_bf16_f32 v17, v22, v23
	v_cndmask_b32_e32 v19, v56, v16, vcc
	v_cndmask_b32_e32 v18, v57, v17, vcc
	v_cndmask_b32_e32 v20, v34, v25, vcc
	v_cndmask_b32_e32 v21, v33, v24, vcc
	ds_bpermute_b32 v19, v35, v19
	ds_bpermute_b32 v22, v35, v18
	ds_bpermute_b32 v21, v35, v21
	ds_bpermute_b32 v26, v35, v20
	s_waitcnt lgkmcnt(3)
	v_cndmask_b32_e32 v18, v16, v19, vcc
	v_cndmask_b32_e32 v16, v19, v56, vcc
	s_waitcnt lgkmcnt(2)
	v_cndmask_b32_e32 v19, v17, v22, vcc
	v_cndmask_b32_e32 v17, v22, v57, vcc
	s_waitcnt lgkmcnt(1)
	v_cndmask_b32_e32 v22, v24, v21, vcc
	v_cndmask_b32_e32 v20, v21, v33, vcc
	s_waitcnt lgkmcnt(0)
	v_cndmask_b32_e32 v23, v25, v26, vcc
	v_cndmask_b32_e32 v21, v26, v34, vcc
	ds_read_b128 v[24:27], v32 offset:4096
	ds_read_b128 v[28:31], v32 offset:12288
	global_store_dwordx4 v[68:69], v[20:23], off offset:1024
	global_store_dwordx4 v[46:47], v[16:19], off offset:1024
	s_nop 0
	v_pk_mul_f32 v[20:21], v[50:51], v[82:83] op_sel_hi:[1,0]
	v_pk_mul_f32 v[16:17], v[48:49], v[82:83] op_sel_hi:[1,0]
	v_pk_mul_f32 v[18:19], v[54:55], v[82:83] op_sel_hi:[1,0]
	s_waitcnt lgkmcnt(0)
	v_pk_fma_f32 v[16:17], v[16:17], v[24:25], v[28:29]
	v_pk_fma_f32 v[18:19], v[18:19], v[26:27], v[30:31]
	v_cvt_pk_f16_f32 v24, v12, v13
	v_cvt_pk_f16_f32 v25, v14, v15
	v_cvt_pk_bf16_f32 v26, v16, v17
	v_pk_mul_f32 v[22:23], v[40:41], v[82:83] op_sel_hi:[1,0]
	v_cvt_pk_bf16_f32 v27, v18, v19
	ds_read_b128 v[12:15], v32 offset:5120
	ds_read_b128 v[16:19], v32 offset:13312
	s_waitcnt lgkmcnt(0)
	v_pk_fma_f32 v[12:13], v[20:21], v[12:13], v[16:17]
	v_pk_fma_f32 v[14:15], v[22:23], v[14:15], v[18:19]
	v_cvt_pk_f16_f32 v16, v8, v9
	v_cvt_pk_f16_f32 v17, v10, v11
	v_cvt_pk_bf16_f32 v8, v12, v13
	s_nop 0
	v_cvt_pk_bf16_f32 v9, v14, v15
	v_cndmask_b32_e32 v11, v26, v8, vcc
	v_cndmask_b32_e32 v10, v27, v9, vcc
	v_cndmask_b32_e32 v12, v25, v17, vcc
	v_cndmask_b32_e32 v13, v24, v16, vcc
	ds_bpermute_b32 v11, v35, v11
	ds_bpermute_b32 v14, v35, v10
	ds_bpermute_b32 v13, v35, v13
	ds_bpermute_b32 v18, v35, v12
	s_waitcnt lgkmcnt(3)
	v_cndmask_b32_e32 v10, v8, v11, vcc
	v_cndmask_b32_e32 v8, v11, v26, vcc
	s_waitcnt lgkmcnt(2)
	v_cndmask_b32_e32 v11, v9, v14, vcc
	v_cndmask_b32_e32 v9, v14, v27, vcc
	s_waitcnt lgkmcnt(1)
	v_cndmask_b32_e32 v14, v16, v13, vcc
	v_cndmask_b32_e32 v12, v13, v24, vcc
	s_waitcnt lgkmcnt(0)
	v_cndmask_b32_e32 v15, v17, v18, vcc
	v_cndmask_b32_e32 v13, v18, v25, vcc
	ds_read_b128 v[16:19], v32 offset:6144
	ds_read_b128 v[20:23], v32 offset:14336
	global_store_dwordx4 v[68:69], v[12:15], off offset:2048
	global_store_dwordx4 v[46:47], v[8:11], off offset:2048
	s_nop 0
	v_pk_mul_f32 v[12:13], v[36:37], v[82:83] op_sel_hi:[1,0]
	v_pk_mul_f32 v[8:9], v[42:43], v[82:83] op_sel_hi:[1,0]
	v_pk_mul_f32 v[10:11], v[38:39], v[82:83] op_sel_hi:[1,0]
	s_waitcnt lgkmcnt(0)
	v_pk_fma_f32 v[8:9], v[8:9], v[16:17], v[20:21]
	v_pk_fma_f32 v[10:11], v[10:11], v[18:19], v[22:23]
	v_cvt_pk_f16_f32 v16, v4, v5
	v_cvt_pk_f16_f32 v17, v6, v7
	v_cvt_pk_bf16_f32 v18, v8, v9
	v_pk_mul_f32 v[14:15], v[44:45], v[82:83] op_sel_hi:[1,0]
	v_cvt_pk_bf16_f32 v19, v10, v11
	ds_read_b128 v[4:7], v32 offset:7168
	ds_read_b128 v[8:11], v32 offset:15360
	s_waitcnt lgkmcnt(0)
	v_pk_fma_f32 v[4:5], v[12:13], v[4:5], v[8:9]
	v_pk_fma_f32 v[6:7], v[14:15], v[6:7], v[10:11]
	v_cvt_pk_f16_f32 v8, v0, v1
	v_cvt_pk_f16_f32 v9, v2, v3
	v_cvt_pk_bf16_f32 v0, v4, v5
	s_nop 0
	v_cvt_pk_bf16_f32 v1, v6, v7
	v_cndmask_b32_e32 v3, v18, v0, vcc
	v_cndmask_b32_e32 v2, v19, v1, vcc
	v_cndmask_b32_e32 v4, v17, v9, vcc
	v_cndmask_b32_e32 v5, v16, v8, vcc
	ds_bpermute_b32 v3, v35, v3
	ds_bpermute_b32 v6, v35, v2
	ds_bpermute_b32 v5, v35, v5
	ds_bpermute_b32 v10, v35, v4
	s_waitcnt lgkmcnt(3)
	v_cndmask_b32_e32 v2, v0, v3, vcc
	v_cndmask_b32_e32 v0, v3, v18, vcc
	s_waitcnt lgkmcnt(2)
	v_cndmask_b32_e32 v3, v1, v6, vcc
	v_cndmask_b32_e32 v1, v6, v19, vcc
	s_waitcnt lgkmcnt(1)
	v_cndmask_b32_e32 v6, v8, v5, vcc
	v_cndmask_b32_e32 v4, v5, v16, vcc
	s_waitcnt lgkmcnt(0)
	v_cndmask_b32_e32 v7, v9, v10, vcc
	v_cndmask_b32_e32 v5, v10, v17, vcc
	global_store_dwordx4 v[68:69], v[4:7], off offset:3072
	global_store_dwordx4 v[46:47], v[0:3], off offset:3072

	.amdhsa_kernel _Z11prep_kernel7CvtArgsPKiPj6LnArgs
		.amdhsa_group_segment_fixed_size 16896
		.amdhsa_private_segment_fixed_size 0
		.amdhsa_kernarg_size 464
		.amdhsa_user_sgpr_count 2
		.amdhsa_user_sgpr_dispatch_ptr 0
		.amdhsa_user_sgpr_queue_ptr 0
		.amdhsa_user_sgpr_kernarg_segment_ptr 1
		.amdhsa_user_sgpr_dispatch_id 0
		.amdhsa_user_sgpr_kernarg_preload_length 0
		.amdhsa_user_sgpr_kernarg_preload_offset 0
		.amdhsa_user_sgpr_private_segment_size 0
		.amdhsa_uses_dynamic_stack 0
		.amdhsa_enable_private_segment 0
		.amdhsa_system_sgpr_workgroup_id_x 1
		.amdhsa_system_sgpr_workgroup_id_y 0
		.amdhsa_system_sgpr_workgroup_id_z 0
		.amdhsa_system_sgpr_workgroup_info 0
		.amdhsa_system_vgpr_workitem_id 2
		.amdhsa_next_free_vgpr 120
		.amdhsa_next_free_sgpr 56
		.amdhsa_accum_offset 120
		.amdhsa_reserve_vcc 1
		.amdhsa_float_round_mode_32 0
		.amdhsa_float_round_mode_16_64 0
		.amdhsa_float_denorm_mode_32 3
		.amdhsa_float_denorm_mode_16_64 3
		.amdhsa_dx10_clamp 1
		.amdhsa_ieee_mode 1
		.amdhsa_fp16_overflow 0
		.amdhsa_tg_split 0
		.amdhsa_exception_fp_ieee_invalid_op 0
		.amdhsa_exception_fp_denorm_src 0
		.amdhsa_exception_fp_ieee_div_zero 0
		.amdhsa_exception_fp_ieee_overflow 0
		.amdhsa_exception_fp_ieee_underflow 0
		.amdhsa_exception_fp_ieee_inexact 0
		.amdhsa_exception_int_div_zero 0
	.end_amdhsa_kernel

_Z6gemm4pILi96ELi2ELi0EEvPKtS1_iii7EpiArgs:
	s_load_dwordx4 s[4:7], s[0:1], 0x10
	s_load_dwordx2 s[8:9], s[0:1], 0x8
	s_waitcnt lgkmcnt(0)
	s_mov_b32 s62, s2
	s_add_u32 s84, s8, 0xe3a0100
	s_addc_u32 s85, s9, 0
	s_load_dwordx4 s[64:67], s[84:85], 0x0
	s_mul_i32 s63, s62, 0x6200
	s_add_u32 s68, s8, 0x2d60000
	s_addc_u32 s69, s9, 0
	s_add_u32 s68, s68, s63
	s_addc_u32 s69, s69, 0
	s_mul_i32 s63, s62, 0x4200
	s_add_u32 s70, s8, 0x18c0000
	s_addc_u32 s71, s9, 0
	s_add_u32 s70, s70, s63
	s_addc_u32 s71, s71, 0
	v_lshlrev_b32_e32 v216, 4, v0
	v_mov_b32_e32 v217, v0
	s_mov_b32 s79, 0xaaab
	s_mov_b32 s80, 0x10000
	s_ashr_i32 s3, s4, 31
	s_lshr_b32 s3, s3, 24
	s_mul_hi_i32 s5, s5, 0x2aaaaaab
	s_add_i32 s3, s4, s3
	s_ashr_i32 s10, s3, 8
	s_lshr_b32 s3, s5, 31
	s_ashr_i32 s7, s5, 5
	s_add_i32 s7, s7, s3
	s_mul_i32 s4, s7, s10
	s_ashr_i32 s3, s4, 31
	s_lshr_b32 s3, s3, 29
	s_add_i32 s5, s4, s3
	s_ashr_i32 s3, s5, 3
	s_and_b32 s5, s5, -8
	s_sub_i32 s4, s4, s5
	s_ashr_i32 s5, s2, 31
	s_lshr_b32 s5, s5, 29
	s_add_i32 s14, s2, s5
	s_and_b32 s5, s14, -8
	s_sub_i32 s12, s2, s5
	s_add_i32 s13, s3, 1
	s_cmp_ge_i32 s12, s4
	s_cbranch_scc0 .LBB2_2
	s_mul_i32 s2, s13, s4
	s_sub_i32 s4, s12, s4
	s_mul_i32 s4, s4, s3
	s_add_i32 s11, s2, s4
	s_load_dwordx2 s[2:3], s[0:1], 0x0
	s_ashr_i32 s4, s14, 3
	s_cbranch_execz .LBB2_3
	s_branch .LBB2_4

.LBB2_6:
	s_mul_i32 s18, s18, s16
	s_sub_i32 s5, s17, s18
	s_add_i32 s5, s5, s7
	s_lshl_b32 s7, s5, 8
	s_ashr_i32 s8, s7, 31
	s_mul_i32 s8, s10, s8
	s_mul_hi_u32 s9, s10, s7
	v_mul_lo_u32 v7, v1, s4
	v_add_u32_e32 v1, 64, v1
	s_add_i32 s8, s9, s8
	s_mul_i32 s9, s11, s7
	s_lshl_b32 s5, s4, 2
	v_lshrrev_b32_e32 v1, 1, v1
	s_add_i32 s8, s8, s9
	s_mul_i32 s9, s10, s7
	v_xor_b32_e32 v1, v1, v0
	s_waitcnt lgkmcnt(0)
	s_mul_i32 s63, s62, 0xc000
	s_add_u32 s66, s66, s63
	s_addc_u32 s67, s67, 0
	s_lshl_b32 s63, s62, 15
	s_add_u32 s64, s64, s63
	s_addc_u32 s65, s65, 0
	s_sub_u32 s64, s64, 0xc000
	s_subb_u32 s65, s65, 0
	s_add_u32 s16, s2, s9
	v_add_u32_e32 v4, s5, v4
	v_lshlrev_b32_e32 v1, 3, v1
	s_addc_u32 s2, s3, s8
	s_mov_b32 m0, s28
	v_add_lshl_u32 v180, v3, v7, 1
	v_add_lshl_u32 v179, v4, v3, 1
	v_lshl_add_u32 v3, s4, 6, v7
	v_and_b32_e32 v1, 56, v1
	s_and_b32 s17, s2, 0xffff
	s_mov_b32 s18, s14
	s_mov_b32 s19, s15
	s_add_i32 s33, s28, 0x2000
	v_add_lshl_u32 v181, v1, v3, 1
	buffer_load_dwordx4 v180, s[16:19], 0 offen lds
	s_mov_b32 m0, s33
	s_add_i32 s34, s28, 0x4000
	s_lshl_b32 s29, s4, 8
	buffer_load_dwordx4 v181, s[16:19], 0 offen lds
	s_mov_b32 m0, s34
	s_add_i32 s35, s28, 0x6000
	buffer_load_dwordx4 v180, s[16:19], s29 offen lds
	s_mov_b32 m0, s35
	s_add_i32 s36, s28, 0x13000
	buffer_load_dwordx4 v181, s[16:19], s29 offen lds
	s_mov_b32 m0, s36
	s_and_b32 s2, s30, 0xffffff00
	buffer_load_dwordx4 v179, s[12:15], 0 offen lds
	v_add_u32_e32 v1, s5, v6
	s_cmpk_eq_i32 s2, 0x100
	s_cselect_b64 s[22:23], -1, 0
	s_cmpk_lg_i32 s2, 0x100
	v_add_lshl_u32 v182, v1, v5, 1
	s_cbranch_scc1 .LBB2_8
	s_lshl_b32 s2, s27, 10
	s_add_i32 s2, s2, 0
	s_add_i32 m0, s2, 0x13000
	s_nop 0
	buffer_load_dwordx4 v182, s[12:15], 0 offen lds
	s_barrier

.LBB2_12:
	s_mov_b32 m0, s38
	s_nop 0
	buffer_load_dwordx4 v180, s[16:19], s59 offen lds
	s_mov_b32 m0, s39
	s_nop 0
	buffer_load_dwordx4 v181, s[16:19], s59 offen lds
	s_waitcnt vmcnt(5)
	s_waitcnt lgkmcnt(0)
	s_barrier
	s_setprio 1
	s_waitcnt lgkmcnt(5)
	v_mfma_f32_16x16x32_bf16 v[42:45], v[134:137], v[106:109], v[42:45]
	s_waitcnt lgkmcnt(3)
	v_mfma_f32_16x16x32_bf16 v[34:37], v[142:145], v[106:109], v[34:37]
	s_waitcnt lgkmcnt(1)
	v_mfma_f32_16x16x32_bf16 v[26:29], v[150:153], v[106:109], v[26:29]
	v_mfma_f32_16x16x32_bf16 v[106:109], v[150:153], v[122:125], v[30:33]
	v_mfma_f32_16x16x32_bf16 v[162:165], v[134:137], v[122:125], v[46:49]
	s_waitcnt lgkmcnt(0)
	v_mfma_f32_16x16x32_bf16 v[30:33], v[146:149], v[110:113], v[26:29]
	s_cmp_lt_u32 s72, 6
	s_cselect_b32 s76, s68, s70
	s_cselect_b32 s77, s69, s71
	s_cselect_b32 s78, s79, s80
	s_cselect_b32 s81, 0, 6
	s_sub_u32 s81, s72, s81
	s_lshl_b32 s81, s81, 9
	v_add_u32_e32 v222, s81, v217
	v_mul_u32_u24_e32 v223, s78, v222
	v_lshrrev_b32_e32 v223, 25, v223
	v_lshlrev_b32_e32 v222, 3, v222
	v_lshl_add_u32 v222, v223, 7, v222
	s_cmp_lt_u32 s72, 6
	s_cbranch_scc0 .Lqkv_cvt_bf
	v_cvt_pk_f16_f32 v224, v218, v219
	v_cvt_pk_f16_f32 v225, v220, v221
	s_branch .Lqkv_cvt_done
.Lqkv_cvt_bf:
	v_cvt_pk_bf16_f32 v224, v218, v219
	v_cvt_pk_bf16_f32 v225, v220, v221
.Lqkv_cvt_done:
	global_store_dwordx2 v222, v[224:225], s[76:77]
	v_mfma_f32_16x16x32_bf16 v[26:29], v[146:149], v[126:129], v[106:109]
	v_mfma_f32_16x16x32_bf16 v[18:21], v[134:137], v[98:101], v[18:21]
	v_mfma_f32_16x16x32_bf16 v[106:109], v[134:137], v[114:117], v[22:25]
	v_mfma_f32_16x16x32_bf16 v[46:49], v[130:133], v[110:113], v[42:45]
	v_mfma_f32_16x16x32_bf16 v[42:45], v[130:133], v[126:129], v[162:165]
	v_mfma_f32_16x16x32_bf16 v[162:165], v[142:145], v[122:125], v[38:41]
	v_mfma_f32_16x16x32_bf16 v[22:25], v[130:133], v[102:105], v[18:21]
	v_mfma_f32_16x16x32_bf16 v[18:21], v[130:133], v[118:121], v[106:109]
	v_mfma_f32_16x16x32_bf16 v[10:13], v[142:145], v[98:101], v[10:13]
	v_mfma_f32_16x16x32_bf16 v[106:109], v[142:145], v[114:117], v[14:17]
	v_mfma_f32_16x16x32_bf16 v[2:5], v[150:153], v[98:101], v[2:5]
	v_mfma_f32_16x16x32_bf16 v[98:101], v[150:153], v[114:117], v[6:9]
	v_mfma_f32_16x16x32_bf16 v[38:41], v[138:141], v[110:113], v[34:37]
	v_mfma_f32_16x16x32_bf16 v[34:37], v[138:141], v[126:129], v[162:165]
	v_mfma_f32_16x16x32_bf16 v[14:17], v[138:141], v[102:105], v[10:13]
	v_mfma_f32_16x16x32_bf16 v[10:13], v[138:141], v[118:121], v[106:109]
	v_mfma_f32_16x16x32_bf16 v[6:9], v[146:149], v[102:105], v[2:5]
	v_mfma_f32_16x16x32_bf16 v[2:5], v[146:149], v[118:121], v[98:101]
	s_setprio 0
	s_barrier
	s_add_i32 s42, s42, 2
	s_addk_i32 s50, 0x100
	s_cmp_ge_i32 s42, s40
	s_cbranch_scc1 .LBB2_21

.LBB2_15:
	s_add_i32 s60, s50, 0xffffc000
	ds_read_b128 v[122:125], v187 offset:16384
	ds_read_b128 v[114:117], v187 offset:18432
	ds_read_b128 v[126:129], v186 offset:16384
	ds_read_b128 v[118:121], v186 offset:18432
	s_waitcnt vmcnt(7)
	s_waitcnt lgkmcnt(4)
	s_barrier
	s_setprio 1
	v_mfma_f32_16x16x32_bf16 v[94:97], v[150:153], v[106:109], v[94:97]
	v_mfma_f32_16x16x32_bf16 v[86:89], v[142:145], v[106:109], v[86:89]
	v_mfma_f32_16x16x32_bf16 v[78:81], v[134:137], v[106:109], v[78:81]
	v_mfma_f32_16x16x32_bf16 v[70:73], v[150:153], v[98:101], v[70:73]
	v_mfma_f32_16x16x32_bf16 v[62:65], v[142:145], v[98:101], v[62:65]
	v_mfma_f32_16x16x32_bf16 v[54:57], v[134:137], v[98:101], v[54:57]
	s_lshr_b32 s72, s42, 1
	s_min_u32 s72, s72, 9
	s_lshl_b32 s73, s72, 13
	s_cmp_lt_u32 s72, 6
	s_cselect_b32 s74, s66, s64
	s_cselect_b32 s75, s67, s65
	s_add_u32 s74, s74, s73
	s_addc_u32 s75, s75, 0
	global_load_dwordx4 v[218:221], v216, s[74:75] nt
	v_mfma_f32_16x16x32_bf16 v[94:97], v[146:149], v[110:113], v[94:97]
	v_mfma_f32_16x16x32_bf16 v[86:89], v[138:141], v[110:113], v[86:89]
	v_mfma_f32_16x16x32_bf16 v[78:81], v[130:133], v[110:113], v[78:81]
	v_mfma_f32_16x16x32_bf16 v[70:73], v[146:149], v[102:105], v[70:73]
	v_mfma_f32_16x16x32_bf16 v[62:65], v[138:141], v[102:105], v[62:65]
	v_mfma_f32_16x16x32_bf16 v[54:57], v[130:133], v[102:105], v[54:57]
	s_waitcnt lgkmcnt(2)
	v_mfma_f32_16x16x32_bf16 v[90:93], v[150:153], v[122:125], v[90:93]
	v_mfma_f32_16x16x32_bf16 v[82:85], v[142:145], v[122:125], v[82:85]
	v_mfma_f32_16x16x32_bf16 v[74:77], v[134:137], v[122:125], v[74:77]
	v_mfma_f32_16x16x32_bf16 v[66:69], v[150:153], v[114:117], v[66:69]
	v_mfma_f32_16x16x32_bf16 v[58:61], v[142:145], v[114:117], v[58:61]
	v_mfma_f32_16x16x32_bf16 v[50:53], v[134:137], v[114:117], v[50:53]
	s_waitcnt lgkmcnt(0)
	v_mfma_f32_16x16x32_bf16 v[90:93], v[146:149], v[126:129], v[90:93]
	v_mfma_f32_16x16x32_bf16 v[82:85], v[138:141], v[126:129], v[82:85]
	v_mfma_f32_16x16x32_bf16 v[74:77], v[130:133], v[126:129], v[74:77]
	v_mfma_f32_16x16x32_bf16 v[66:69], v[146:149], v[118:121], v[66:69]
	v_mfma_f32_16x16x32_bf16 v[58:61], v[138:141], v[118:121], v[58:61]
	v_mfma_f32_16x16x32_bf16 v[50:53], v[130:133], v[118:121], v[50:53]
	s_setprio 0
	s_barrier
	s_mov_b32 m0, s31
	v_add_u32_e32 v130, s51, v184
	v_add_u32_e32 v131, s51, v185
	v_add_u32_e32 v138, s52, v184
	v_add_u32_e32 v139, s52, v185
	v_add_u32_e32 v146, s53, v184
	v_add_u32_e32 v147, s53, v185
	ds_read_b128 v[134:137], v130
	ds_read_b128 v[130:133], v131
	ds_read_b128 v[142:145], v138
	ds_read_b128 v[138:141], v139
	ds_read_b128 v[150:153], v146
	ds_read_b128 v[146:149], v147
	buffer_load_dwordx4 v154, s[12:15], s60 offen lds
	s_and_b64 vcc, exec, s[4:5]
	s_cbranch_vccnz .LBB2_17
	s_mov_b32 m0, s46
	s_nop 0
	buffer_load_dwordx4 v155, s[12:15], s60 offen lds
.LBB2_17:
	s_mov_b32 m0, s28
	s_nop 0
	buffer_load_dwordx4 v180, s[16:19], s60 offen lds
	s_mov_b32 m0, s33
	s_nop 0
	buffer_load_dwordx4 v181, s[16:19], s60 offen lds
	s_waitcnt vmcnt(6)
	s_waitcnt lgkmcnt(0)
	s_barrier
	s_setprio 1
	s_waitcnt lgkmcnt(5)
	v_mfma_f32_16x16x32_bf16 v[46:49], v[134:137], v[106:109], v[46:49]
	s_waitcnt lgkmcnt(3)
	v_mfma_f32_16x16x32_bf16 v[38:41], v[142:145], v[106:109], v[38:41]
	s_waitcnt lgkmcnt(1)
	v_mfma_f32_16x16x32_bf16 v[30:33], v[150:153], v[106:109], v[30:33]
	v_mfma_f32_16x16x32_bf16 v[106:109], v[150:153], v[122:125], v[26:29]
	v_mfma_f32_16x16x32_bf16 v[162:165], v[134:137], v[122:125], v[42:45]
	s_waitcnt lgkmcnt(0)
	v_mfma_f32_16x16x32_bf16 v[26:29], v[146:149], v[110:113], v[30:33]
	v_mfma_f32_16x16x32_bf16 v[30:33], v[146:149], v[126:129], v[106:109]
	v_mfma_f32_16x16x32_bf16 v[22:25], v[134:137], v[98:101], v[22:25]
	v_mfma_f32_16x16x32_bf16 v[106:109], v[134:137], v[114:117], v[18:21]
	v_mfma_f32_16x16x32_bf16 v[42:45], v[130:133], v[110:113], v[46:49]
	v_mfma_f32_16x16x32_bf16 v[46:49], v[130:133], v[126:129], v[162:165]
	v_mfma_f32_16x16x32_bf16 v[162:165], v[142:145], v[122:125], v[34:37]
	v_mfma_f32_16x16x32_bf16 v[18:21], v[130:133], v[102:105], v[22:25]
	v_mfma_f32_16x16x32_bf16 v[22:25], v[130:133], v[118:121], v[106:109]
	v_mfma_f32_16x16x32_bf16 v[14:17], v[142:145], v[98:101], v[14:17]
	v_mfma_f32_16x16x32_bf16 v[106:109], v[142:145], v[114:117], v[10:13]
	v_mfma_f32_16x16x32_bf16 v[6:9], v[150:153], v[98:101], v[6:9]
	v_mfma_f32_16x16x32_bf16 v[98:101], v[150:153], v[114:117], v[2:5]
	v_mfma_f32_16x16x32_bf16 v[34:37], v[138:141], v[110:113], v[38:41]
	v_mfma_f32_16x16x32_bf16 v[38:41], v[138:141], v[126:129], v[162:165]
	v_mfma_f32_16x16x32_bf16 v[10:13], v[138:141], v[102:105], v[14:17]
	v_mfma_f32_16x16x32_bf16 v[14:17], v[138:141], v[118:121], v[106:109]
	v_mfma_f32_16x16x32_bf16 v[2:5], v[146:149], v[102:105], v[6:9]
	v_mfma_f32_16x16x32_bf16 v[6:9], v[146:149], v[118:121], v[98:101]
	s_setprio 0
	s_barrier
	s_nop 0
	v_add_u32_e32 v98, s54, v184
	v_add_u32_e32 v99, s54, v185
	ds_read_b128 v[134:137], v98
	ds_read_b128 v[130:133], v99
	v_add_u32_e32 v98, s55, v184
	v_add_u32_e32 v99, s55, v185
	ds_read_b128 v[142:145], v98
	ds_read_b128 v[138:141], v99
	v_add_u32_e32 v98, s56, v184
	v_add_u32_e32 v99, s56, v185
	ds_read_b128 v[150:153], v98
	ds_read_b128 v[146:149], v99
	s_mov_b32 m0, s34
	s_nop 0
	buffer_load_dwordx4 v180, s[16:19], s59 offen lds
	s_mov_b32 m0, s35
	s_nop 0
	buffer_load_dwordx4 v181, s[16:19], s59 offen lds
	ds_read_b128 v[106:109], v187 offset:32768
	ds_read_b128 v[98:101], v187 offset:34816
	ds_read_b128 v[110:113], v186 offset:32768
	ds_read_b128 v[102:105], v186 offset:34816
	s_mov_b32 m0, s36
	s_and_b64 vcc, exec, s[2:3]
	buffer_load_dwordx4 v179, s[12:15], s60 offen lds
	s_cbranch_vccnz .LBB2_19
	s_mov_b32 m0, s47
	s_nop 0
	buffer_load_dwordx4 v182, s[12:15], s60 offen lds
.LBB2_19:
	s_add_i32 s59, s50, 0xffffc080
	ds_read_b128 v[122:125], v187 offset:49152
	ds_read_b128 v[114:117], v187 offset:51200
	ds_read_b128 v[126:129], v186 offset:49152
	ds_read_b128 v[118:121], v186 offset:51200
	s_waitcnt vmcnt(8)
	s_waitcnt lgkmcnt(4)
	s_barrier
	s_setprio 1
	v_mfma_f32_16x16x32_bf16 v[94:97], v[134:137], v[106:109], v[94:97]
	v_mfma_f32_16x16x32_bf16 v[70:73], v[134:137], v[98:101], v[70:73]
	v_mfma_f32_16x16x32_bf16 v[86:89], v[142:145], v[106:109], v[86:89]
	v_mfma_f32_16x16x32_bf16 v[62:65], v[142:145], v[98:101], v[62:65]
	v_mfma_f32_16x16x32_bf16 v[78:81], v[150:153], v[106:109], v[78:81]
	v_mfma_f32_16x16x32_bf16 v[54:57], v[150:153], v[98:101], v[54:57]
	v_mfma_f32_16x16x32_bf16 v[94:97], v[130:133], v[110:113], v[94:97]
	v_mfma_f32_16x16x32_bf16 v[70:73], v[130:133], v[102:105], v[70:73]
	v_mfma_f32_16x16x32_bf16 v[86:89], v[138:141], v[110:113], v[86:89]
	v_mfma_f32_16x16x32_bf16 v[62:65], v[138:141], v[102:105], v[62:65]
	v_mfma_f32_16x16x32_bf16 v[78:81], v[146:149], v[110:113], v[78:81]
	v_mfma_f32_16x16x32_bf16 v[54:57], v[146:149], v[102:105], v[54:57]
	s_waitcnt lgkmcnt(2)
	v_mfma_f32_16x16x32_bf16 v[90:93], v[134:137], v[122:125], v[90:93]
	v_mfma_f32_16x16x32_bf16 v[66:69], v[134:137], v[114:117], v[66:69]
	v_mfma_f32_16x16x32_bf16 v[82:85], v[142:145], v[122:125], v[82:85]
	v_mfma_f32_16x16x32_bf16 v[58:61], v[142:145], v[114:117], v[58:61]
	v_mfma_f32_16x16x32_bf16 v[74:77], v[150:153], v[122:125], v[74:77]
	v_mfma_f32_16x16x32_bf16 v[50:53], v[150:153], v[114:117], v[50:53]
	s_waitcnt lgkmcnt(0)
	v_mfma_f32_16x16x32_bf16 v[90:93], v[130:133], v[126:129], v[90:93]
	v_mfma_f32_16x16x32_bf16 v[66:69], v[130:133], v[118:121], v[66:69]
	v_mfma_f32_16x16x32_bf16 v[82:85], v[138:141], v[126:129], v[82:85]
	v_mfma_f32_16x16x32_bf16 v[58:61], v[138:141], v[118:121], v[58:61]
	v_mfma_f32_16x16x32_bf16 v[74:77], v[146:149], v[126:129], v[74:77]
	v_mfma_f32_16x16x32_bf16 v[50:53], v[146:149], v[118:121], v[50:53]
	s_setprio 0
	s_barrier
	s_mov_b32 m0, s37
	s_nop 0
	v_add_u32_e32 v130, s43, v184
	v_add_u32_e32 v131, s43, v185
	v_add_u32_e32 v138, s57, v184
	v_add_u32_e32 v139, s57, v185
	v_add_u32_e32 v146, s58, v184
	v_add_u32_e32 v147, s58, v185
	ds_read_b128 v[134:137], v130
	ds_read_b128 v[130:133], v131
	ds_read_b128 v[142:145], v138
	ds_read_b128 v[138:141], v139
	ds_read_b128 v[150:153], v146
	ds_read_b128 v[146:149], v147
	buffer_load_dwordx4 v154, s[12:15], s59 offen lds
	s_and_b64 vcc, exec, s[4:5]
	s_cbranch_vccnz .LBB2_12
	s_mov_b32 m0, s48
	s_nop 0
	buffer_load_dwordx4 v155, s[12:15], s59 offen lds
	s_branch .LBB2_12

	.amdhsa_kernel _Z6gemm4pILi96ELi2ELi0EEvPKtS1_iii7EpiArgs
		.amdhsa_group_segment_fixed_size 0
		.amdhsa_private_segment_fixed_size 0
		.amdhsa_kernarg_size 104
		.amdhsa_user_sgpr_count 2
		.amdhsa_user_sgpr_dispatch_ptr 0
		.amdhsa_user_sgpr_queue_ptr 0
		.amdhsa_user_sgpr_kernarg_segment_ptr 1
		.amdhsa_user_sgpr_dispatch_id 0
		.amdhsa_user_sgpr_kernarg_preload_length 0
		.amdhsa_user_sgpr_kernarg_preload_offset 0
		.amdhsa_user_sgpr_private_segment_size 0
		.amdhsa_uses_dynamic_stack 0
		.amdhsa_enable_private_segment 0
		.amdhsa_system_sgpr_workgroup_id_x 1
		.amdhsa_system_sgpr_workgroup_id_y 0
		.amdhsa_system_sgpr_workgroup_id_z 0
		.amdhsa_system_sgpr_workgroup_info 0
		.amdhsa_system_vgpr_workitem_id 0
		.amdhsa_next_free_vgpr 228
		.amdhsa_next_free_sgpr 86
		.amdhsa_accum_offset 228
		.amdhsa_reserve_vcc 1
		.amdhsa_float_round_mode_32 0
		.amdhsa_float_round_mode_16_64 0
		.amdhsa_float_denorm_mode_32 3
		.amdhsa_float_denorm_mode_16_64 3
		.amdhsa_dx10_clamp 1
		.amdhsa_ieee_mode 1
		.amdhsa_fp16_overflow 0
		.amdhsa_tg_split 0
		.amdhsa_exception_fp_ieee_invalid_op 0
		.amdhsa_exception_fp_denorm_src 0
		.amdhsa_exception_fp_ieee_div_zero 0
		.amdhsa_exception_fp_ieee_overflow 0
		.amdhsa_exception_fp_ieee_underflow 0
		.amdhsa_exception_fp_ieee_inexact 0
		.amdhsa_exception_int_div_zero 0
	.end_amdhsa_kernel

amdhsa.kernels:
  - .agpr_count:     0
    .args:
      - .offset:         0
        .size:           128
        .value_kind:     by_value
      - .actual_access:  read_only
        .address_space:  global
        .offset:         128
        .size:           8
        .value_kind:     global_buffer
      - .address_space:  global
        .offset:         136
        .size:           8
        .value_kind:     global_buffer
      - .offset:         144
        .size:           64
        .value_kind:     by_value
      - .offset:         208
        .size:           4
        .value_kind:     hidden_block_count_x
      - .offset:         212
        .size:           4
        .value_kind:     hidden_block_count_y
      - .offset:         216
        .size:           4
        .value_kind:     hidden_block_count_z
      - .offset:         220
        .size:           2
        .value_kind:     hidden_group_size_x
      - .offset:         222
        .size:           2
        .value_kind:     hidden_group_size_y
      - .offset:         224
        .size:           2
        .value_kind:     hidden_group_size_z
      - .offset:         226
        .size:           2
        .value_kind:     hidden_remainder_x
      - .offset:         228
        .size:           2
        .value_kind:     hidden_remainder_y
      - .offset:         230
        .size:           2
        .value_kind:     hidden_remainder_z
      - .offset:         248
        .size:           8
        .value_kind:     hidden_global_offset_x
      - .offset:         256
        .size:           8
        .value_kind:     hidden_global_offset_y
      - .offset:         264
        .size:           8
        .value_kind:     hidden_global_offset_z
      - .offset:         272
        .size:           2
        .value_kind:     hidden_grid_dims
    .group_segment_fixed_size: 16896
    .kernarg_segment_align: 8
    .kernarg_segment_size: 464
    .language:       OpenCL C
    .language_version:
      - 2
      - 0
    .max_flat_workgroup_size: 256
    .name:           _Z11prep_kernel7CvtArgsPKiPj6LnArgs
    .private_segment_fixed_size: 0
    .sgpr_count:     62
    .sgpr_spill_count: 0
    .symbol:         _Z11prep_kernel7CvtArgsPKiPj6LnArgs.kd
    .uniform_work_group_size: 1
    .uses_dynamic_stack: false
    .vgpr_count:     120
    .vgpr_spill_count: 0
    .wavefront_size: 64
  - .agpr_count:     0
    .args:
      - .actual_access:  read_only
        .address_space:  global
        .offset:         0
        .size:           8
        .value_kind:     global_buffer
      - .actual_access:  read_only
        .address_space:  global
        .offset:         8
        .size:           8
        .value_kind:     global_buffer
      - .actual_access:  write_only
        .address_space:  global
        .offset:         16
        .size:           8
        .value_kind:     global_buffer
      - .actual_access:  read_only
        .address_space:  global
        .offset:         24
        .size:           8
        .value_kind:     global_buffer
      - .offset:         32
        .size:           4
        .value_kind:     by_value
      - .actual_access:  read_only
        .address_space:  global
        .offset:         40
        .size:           8
        .value_kind:     global_buffer
      - .actual_access:  read_only
        .address_space:  global
        .offset:         48
        .size:           8
        .value_kind:     global_buffer
      - .actual_access:  read_only
        .address_space:  global
        .offset:         56
        .size:           8
        .value_kind:     global_buffer
      - .actual_access:  read_only
        .address_space:  global
        .offset:         64
        .size:           8
        .value_kind:     global_buffer
      - .offset:         72
        .size:           4
        .value_kind:     hidden_block_count_x
      - .offset:         76
        .size:           4
        .value_kind:     hidden_block_count_y
      - .offset:         80
        .size:           4
        .value_kind:     hidden_block_count_z
      - .offset:         84
        .size:           2
        .value_kind:     hidden_group_size_x
      - .offset:         86
        .size:           2
        .value_kind:     hidden_group_size_y
      - .offset:         88
        .size:           2
        .value_kind:     hidden_group_size_z
      - .offset:         90
        .size:           2
        .value_kind:     hidden_remainder_x
      - .offset:         92
        .size:           2
        .value_kind:     hidden_remainder_y
      - .offset:         94
        .size:           2
        .value_kind:     hidden_remainder_z
      - .offset:         112
        .size:           8
        .value_kind:     hidden_global_offset_x
      - .offset:         120
        .size:           8
        .value_kind:     hidden_global_offset_y
      - .offset:         128
        .size:           8
        .value_kind:     hidden_global_offset_z
      - .offset:         136
        .size:           2
        .value_kind:     hidden_grid_dims
    .group_segment_fixed_size: 32768
    .kernarg_segment_align: 8
    .kernarg_segment_size: 328
    .language:       OpenCL C
    .language_version:
      - 2
      - 0
    .max_flat_workgroup_size: 256
    .name:           _ZN4attn12attn_combineEPKfS1_PtPKjiPKtS6_S6_PKi
    .private_segment_fixed_size: 0
    .sgpr_count:     30
    .sgpr_spill_count: 0
    .symbol:         _ZN4attn12attn_combineEPKfS1_PtPKjiPKtS6_S6_PKi.kd
    .uniform_work_group_size: 1
    .uses_dynamic_stack: false
    .vgpr_count:     62
    .vgpr_spill_count: 0
    .wavefront_size: 64
  - .agpr_count:     0
    .args:
      - .actual_access:  read_only
        .address_space:  global
        .offset:         0
        .size:           8
        .value_kind:     global_buffer
      - .actual_access:  read_only
        .address_space:  global
        .offset:         8
        .size:           8
        .value_kind:     global_buffer
      - .offset:         16
        .size:           4
        .value_kind:     by_value
      - .offset:         20
        .size:           4
        .value_kind:     by_value
      - .offset:         24
        .size:           4
        .value_kind:     by_value
      - .offset:         32
        .size:           72
        .value_kind:     by_value
    .group_segment_fixed_size: 0
    .kernarg_segment_align: 8
    .kernarg_segment_size: 104
    .language:       OpenCL C
    .language_version:
      - 2
      - 0
    .max_flat_workgroup_size: 512
    .name:           _Z6gemm4pILi96ELi2ELi0EEvPKtS1_iii7EpiArgs
    .private_segment_fixed_size: 0
    .sgpr_count:     92
    .sgpr_spill_count: 0
    .symbol:         _Z6gemm4pILi96ELi2ELi0EEvPKtS1_iii7EpiArgs.kd
    .uniform_work_group_size: 1
    .uses_dynamic_stack: false
    .vgpr_count:     228
    .vgpr_spill_count: 0
    .wavefront_size: 64
  - .agpr_count:     0
    .args:
      - .actual_access:  read_only
        .address_space:  global
        .offset:         0
        .size:           8
        .value_kind:     global_buffer
      - .actual_access:  read_only
        .address_space:  global
        .offset:         8
        .size:           8
        .value_kind:     global_buffer
      - .actual_access:  read_only
        .address_space:  global
        .offset:         16
        .size:           8
        .value_kind:     global_buffer
      - .actual_access:  write_only
        .address_space:  global
        .offset:         24
        .size:           8
        .value_kind:     global_buffer
      - .actual_access:  write_only
        .address_space:  global
        .offset:         32
        .size:           8
        .value_kind:     global_buffer
      - .actual_access:  write_only
        .address_space:  global
        .offset:         40
        .size:           8
        .value_kind:     global_buffer
      - .actual_access:  read_only
        .address_space:  global
        .offset:         48
        .size:           8
        .value_kind:     global_buffer
      - .actual_access:  write_only
        .address_space:  global
        .offset:         56
        .size:           8
        .value_kind:     global_buffer
      - .offset:         64
        .size:           4
        .value_kind:     by_value
      - .offset:         68
        .size:           4
        .value_kind:     by_value
      - .offset:         72
        .size:           4
        .value_kind:     hidden_block_count_x
      - .offset:         76
        .size:           4
        .value_kind:     hidden_block_count_y
      - .offset:         80
        .size:           4
        .value_kind:     hidden_block_count_z
      - .offset:         84
        .size:           2
        .value_kind:     hidden_group_size_x
      - .offset:         86
        .size:           2
        .value_kind:     hidden_group_size_y
      - .offset:         88
        .size:           2
        .value_kind:     hidden_group_size_z
      - .offset:         90
        .size:           2
        .value_kind:     hidden_remainder_x
      - .offset:         92
        .size:           2
        .value_kind:     hidden_remainder_y
      - .offset:         94
        .size:           2
        .value_kind:     hidden_remainder_z
      - .offset:         112
        .size:           8
        .value_kind:     hidden_global_offset_x
      - .offset:         120
        .size:           8
        .value_kind:     hidden_global_offset_y
      - .offset:         128
        .size:           8
        .value_kind:     hidden_global_offset_z
      - .offset:         136
        .size:           2
        .value_kind:     hidden_grid_dims
      - .offset:         192
        .size:           4
        .value_kind:     hidden_dynamic_lds_size
    .group_segment_fixed_size: 2304
    .kernarg_segment_align: 8
    .kernarg_segment_size: 328
    .language:       OpenCL C
    .language_version:
      - 2
      - 0
    .max_flat_workgroup_size: 512
    .name:           _ZN4attn10attn_splitI14__hip_bfloat16S1_EEvPKT_S4_S4_PT0_PfS7_PKjPjii
    .private_segment_fixed_size: 0
    .sgpr_count:     86
    .sgpr_spill_count: 0
    .symbol:         _ZN4attn10attn_splitI14__hip_bfloat16S1_EEvPKT_S4_S4_PT0_PfS7_PKjPjii.kd
    .uniform_work_group_size: 1
    .uses_dynamic_stack: false
    .vgpr_count:     254
    .vgpr_spill_count: 0
    .wavefront_size: 64
  - .agpr_count:     0
    .args:
      - .actual_access:  read_only
        .address_space:  global
        .offset:         0
        .size:           8
        .value_kind:     global_buffer
      - .actual_access:  read_only
        .address_space:  global
        .offset:         8
        .size:           8
        .value_kind:     global_buffer
      - .offset:         16
        .size:           4
        .value_kind:     by_value
      - .offset:         20
        .size:           4
        .value_kind:     by_value
      - .offset:         24
        .size:           4
        .value_kind:     by_value
      - .offset:         32
        .size:           72
        .value_kind:     by_value
    .group_segment_fixed_size: 0
    .kernarg_segment_align: 8
    .kernarg_segment_size: 104
    .language:       OpenCL C
    .language_version:
      - 2
      - 0
    .max_flat_workgroup_size: 512
    .name:           _Z6gemm4pILi64ELi2ELi3EEvPKtS1_iii7EpiArgs
    .private_segment_fixed_size: 0
    .sgpr_count:     49
    .sgpr_spill_count: 0
    .symbol:         _Z6gemm4pILi64ELi2ELi3EEvPKtS1_iii7EpiArgs.kd
    .uniform_work_group_size: 1
    .uses_dynamic_stack: false
    .vgpr_count:     194
    .vgpr_spill_count: 0
    .wavefront_size: 64
  - .agpr_count:     0
    .args:
      - .actual_access:  read_only
        .address_space:  global
        .offset:         0
        .size:           8
        .value_kind:     global_buffer
      - .actual_access:  read_only
        .address_space:  global
        .offset:         8
        .size:           8
        .value_kind:     global_buffer
      - .offset:         16
        .size:           4
        .value_kind:     by_value
      - .offset:         20
        .size:           4
        .value_kind:     by_value
      - .offset:         24
        .size:           4
        .value_kind:     by_value
      - .offset:         32
        .size:           72
        .value_kind:     by_value
    .group_segment_fixed_size: 0
    .kernarg_segment_align: 8
    .kernarg_segment_size: 104
    .language:       OpenCL C
    .language_version:
      - 2
      - 0
    .max_flat_workgroup_size: 512
    .name:           _Z6gemm4pILi96ELi2ELi4EEvPKtS1_iii7EpiArgs
    .private_segment_fixed_size: 0
    .sgpr_count:     71
    .sgpr_spill_count: 0
    .symbol:         _Z6gemm4pILi96ELi2ELi4EEvPKtS1_iii7EpiArgs.kd
    .uniform_work_group_size: 1
    .uses_dynamic_stack: false
    .vgpr_count:     244
    .vgpr_spill_count: 0
    .wavefront_size: 64
  - .agpr_count:     0
    .args:
      - .actual_access:  read_only
        .address_space:  global
        .offset:         0
        .size:           8
        .value_kind:     global_buffer
      - .actual_access:  read_only
        .address_space:  global
        .offset:         8
        .size:           8
        .value_kind:     global_buffer
      - .offset:         16
        .size:           4
        .value_kind:     by_value
      - .offset:         20
        .size:           4
        .value_kind:     by_value
      - .offset:         24
        .size:           4
        .value_kind:     by_value
      - .offset:         32
        .size:           72
        .value_kind:     by_value
    .group_segment_fixed_size: 0
    .kernarg_segment_align: 8
    .kernarg_segment_size: 104
    .language:       OpenCL C
    .language_version:
      - 2
      - 0
    .max_flat_workgroup_size: 512
    .name:           _Z6gemm4pILi64ELi2ELi1EEvPKtS1_iii7EpiArgs
    .private_segment_fixed_size: 0
    .sgpr_count:     50
    .sgpr_spill_count: 0
    .symbol:         _Z6gemm4pILi64ELi2ELi1EEvPKtS1_iii7EpiArgs.kd
    .uniform_work_group_size: 1
    .uses_dynamic_stack: false
    .vgpr_count:     186
    .vgpr_spill_count: 0
    .wavefront_size: 64
